# baseline (speedup 1.0000x reference)
_Z6k_attnPKDF16_PKfPDF16_:
	s_load_dwordx4 s[4:7], s[0:1], 0x0
	s_load_dwordx2 s[8:9], s[0:1], 0x10
	s_lshr_b32 s0, s2, 3
	s_sub_i32 s0, 0x2ff, s0
	s_lshl_b32 s1, s2, 5
	s_mul_hi_i32 s2, s0, 0x2aaaaaab
	s_lshr_b32 s3, s2, 31
	s_ashr_i32 s2, s2, 2
	s_and_b32 s1, s1, 0xe0
	s_add_i32 s2, s2, s3
	s_add_i32 s1, s2, s1
	s_mul_i32 s2, s2, 24
	s_sub_i32 s0, s0, s2
	s_mul_i32 s2, s0, 43
	s_bfe_u32 s3, s2, 0x1000f
	s_bfe_u32 s2, s2, 0x80008
	s_add_i32 s2, s2, s3
	s_sext_i32_i8 s2, s2
	s_mul_i32 s3, s2, -6
	s_add_i32 s3, s3, s0
	s_lshl_b32 s0, s1, 2
	s_add_i32 s2, s0, s2
	s_mul_i32 s1, s2, 0x48000
	s_mul_hi_i32 s0, s2, 0x48000
	s_waitcnt lgkmcnt(0)
	s_add_u32 s4, s4, s1
	s_addc_u32 s5, s5, s0
	s_lshl_b32 s0, s3, 7
	s_ashr_i32 s1, s0, 31
	s_lshl_b64 s[0:1], s[0:1], 1
	s_add_u32 s4, s4, s0
	v_lshlrev_b32_e32 v2, 4, v0
	v_lshrrev_b32_e32 v9, 4, v0
	s_addc_u32 s5, s5, s1
	v_and_b32_e32 v2, 0xf0, v2
	v_mov_b32_e32 v3, 0
	v_mul_u32_u24_e32 v6, 0x900, v9
	v_lshl_add_u64 v[4:5], s[4:5], 0, v[2:3]
	v_lshlrev_b32_e32 v6, 1, v6
	v_mov_b32_e32 v7, v3
	v_lshl_add_u64 v[6:7], v[4:5], 0, v[6:7]
	global_load_dwordx4 v[10:13], v[6:7], off offset:1536 nt
	global_load_dwordx4 v[14:17], v[6:7], off offset:3072 nt
	v_or_b32_e32 v6, 0x100, v0
	v_lshrrev_b32_e32 v50, 4, v6
	v_mul_u32_u24_e32 v6, 0x900, v50
	v_lshlrev_b32_e32 v6, 1, v6
	v_mov_b32_e32 v7, v3
	v_lshl_add_u64 v[6:7], v[4:5], 0, v[6:7]
	global_load_dwordx4 v[18:21], v[6:7], off offset:1536 nt
	global_load_dwordx4 v[22:25], v[6:7], off offset:3072 nt
	v_or_b32_e32 v6, 0x200, v0
	v_lshrrev_b32_e32 v51, 4, v6
	v_mul_u32_u24_e32 v6, 0x900, v51
	v_lshlrev_b32_e32 v6, 1, v6
	v_mov_b32_e32 v7, v3
	v_lshl_add_u64 v[6:7], v[4:5], 0, v[6:7]
	global_load_dwordx4 v[26:29], v[6:7], off offset:1536 nt
	global_load_dwordx4 v[30:33], v[6:7], off offset:3072 nt
	v_or_b32_e32 v6, 0x300, v0
	v_lshrrev_b32_e32 v52, 4, v6
	v_mul_u32_u24_e32 v6, 0x900, v52
	v_lshlrev_b32_e32 v6, 1, v6
	v_mov_b32_e32 v7, v3
	v_lshrrev_b32_e32 v1, 6, v0
	v_lshl_add_u64 v[4:5], v[4:5], 0, v[6:7]
	v_and_b32_e32 v8, 15, v0
	global_load_dwordx4 v[34:37], v[4:5], off offset:1536 nt
	global_load_dwordx4 v[38:41], v[4:5], off offset:3072 nt
	v_lshlrev_b32_e32 v6, 4, v1
	v_or_b32_e32 v4, v6, v8
	v_mul_u32_u24_e32 v4, 0x900, v4
	v_lshlrev_b32_e32 v4, 1, v4
	v_mov_b32_e32 v5, v3
	v_lshl_add_u64 v[4:5], s[4:5], 0, v[4:5]
	v_and_b32_e32 v58, 48, v0
	v_mov_b32_e32 v59, v3
	v_lshl_add_u64 v[4:5], v[4:5], 0, v[58:59]
	global_load_dwordx4 v[42:45], v[4:5], off nt
	global_load_dwordx4 v[46:49], v[4:5], off offset:64 nt
	s_movk_i32 s3, 0x110
	s_movk_i32 s4, 0x120
	v_or_b32_e32 v7, 0x4800, v2
	v_mad_u32_u24 v59, v9, s4, v2
	v_mad_u32_u24 v9, v9, s3, v7
	v_mad_u32_u24 v60, v50, s4, v2
	v_mad_u32_u24 v61, v51, s4, v2
	v_mad_u32_u24 v62, v52, s4, v2
	v_mad_u32_u24 v63, v50, s3, v7
	v_mad_u32_u24 v64, v51, s3, v7
	v_mad_u32_u24 v7, v52, s3, v7
	global_load_dwordx4 v[50:53], v[4:5], off offset:128 nt
	global_load_dwordx4 v[54:57], v[4:5], off offset:192 nt
	v_lshlrev_b32_e32 v4, 2, v8
	v_mov_b32_e32 v5, v3
	v_lshl_add_u64 v[4:5], s[6:7], 0, v[4:5]
	v_bfe_u32 v84, v0, 4, 2
	v_lshrrev_b32_e32 v85, 6, v0
	v_lshlrev_b32_e32 v84, 2, v84
	v_lshl_or_b32 v84, v85, 4, v84
	v_lshlrev_b32_e32 v84, 8, v84
	v_mov_b32_e32 v85, v3
	v_lshl_add_u64 v[84:85], v[4:5], 0, v[84:85]
	global_load_dword v68, v[84:85], off
	global_load_dword v69, v[84:85], off offset:64
	global_load_dword v70, v[84:85], off offset:128
	global_load_dword v71, v[84:85], off offset:192
	global_load_dword v72, v[84:85], off offset:256
	global_load_dword v73, v[84:85], off offset:320
	global_load_dword v74, v[84:85], off offset:384
	global_load_dword v75, v[84:85], off offset:448
	global_load_dword v76, v[84:85], off offset:512
	global_load_dword v77, v[84:85], off offset:576
	global_load_dword v78, v[84:85], off offset:640
	global_load_dword v79, v[84:85], off offset:704
	global_load_dword v80, v[84:85], off offset:768
	global_load_dword v81, v[84:85], off offset:832
	global_load_dword v82, v[84:85], off offset:896
	global_load_dword v83, v[84:85], off offset:960
	s_movk_i32 s4, 0x900
	s_waitcnt vmcnt(27)
	ds_write_b128 v9, v[10:13]
	s_waitcnt vmcnt(26)
	ds_write_b128 v59, v[14:17]
	s_waitcnt vmcnt(25)
	ds_write_b128 v63, v[18:21]
	s_waitcnt vmcnt(24)
	ds_write_b128 v60, v[22:25]
	s_waitcnt vmcnt(23)
	ds_write_b128 v64, v[26:29]
	s_waitcnt vmcnt(22)
	ds_write_b128 v61, v[30:33]
	s_waitcnt vmcnt(21)
	ds_write_b128 v7, v[34:37]
	s_waitcnt vmcnt(20)
	ds_write_b128 v62, v[38:41]
	v_mad_u32_u24 v30, v8, s3, v58
	s_waitcnt lgkmcnt(0)
	s_barrier
	ds_read_b128 v[10:13], v30 offset:18432
	ds_read_b128 v[14:17], v30 offset:18496
	s_waitcnt vmcnt(19) lgkmcnt(1)
	v_mfma_f32_16x16x32_f16 a[0:3], v[42:45], v[10:13], 0
	v_bfe_u32 v7, v0, 4, 2
	v_lshlrev_b32_e32 v9, 2, v7
	v_mbcnt_lo_u32_b32 v39, -1, 0
	s_waitcnt vmcnt(18) lgkmcnt(0)
	v_mfma_f32_16x16x32_f16 a[0:3], v[46:49], v[14:17], a[0:3]
	ds_read_b128 v[10:13], v30 offset:22784
	ds_read_b128 v[14:17], v30 offset:22848
	s_waitcnt lgkmcnt(1)
	v_mfma_f32_16x16x32_f16 a[4:7], v[42:45], v[10:13], 0
	s_waitcnt lgkmcnt(0)
	v_mfma_f32_16x16x32_f16 a[4:7], v[46:49], v[14:17], a[4:7]
	ds_read_b128 v[10:13], v30 offset:27136
	ds_read_b128 v[14:17], v30 offset:27200
	s_waitcnt lgkmcnt(1)
	v_mfma_f32_16x16x32_f16 a[8:11], v[42:45], v[10:13], 0
	ds_read_b128 v[10:13], v30 offset:31488
	s_waitcnt lgkmcnt(1)
	v_mfma_f32_16x16x32_f16 a[8:11], v[46:49], v[14:17], a[8:11]
	ds_read_b128 v[14:17], v30 offset:31552
	s_waitcnt lgkmcnt(1)
	v_mfma_f32_16x16x32_f16 a[12:15], v[42:45], v[10:13], 0
	v_or_b32_e32 v10, v9, v6
	v_lshlrev_b32_e32 v10, 8, v10
	v_mov_b32_e32 v11, v3
	v_lshl_add_u64 v[4:5], v[4:5], 0, v[10:11]
	s_waitcnt lgkmcnt(0)
	v_mfma_f32_16x16x32_f16 a[12:15], v[46:49], v[14:17], a[12:15]
	ds_read_b128 v[10:13], v30 offset:18560
	ds_read_b128 v[14:17], v30 offset:18624
	ds_read_b128 v[18:21], v30 offset:22912
	s_waitcnt vmcnt(17) lgkmcnt(2)
	v_mfma_f32_16x16x32_f16 a[0:3], v[50:53], v[10:13], a[0:3]
	ds_read_b128 v[10:13], v30 offset:22976
	ds_read_b128 v[22:25], v30 offset:27264
	ds_read_b128 v[26:29], v30 offset:27328
	s_waitcnt lgkmcnt(3)
	v_mfma_f32_16x16x32_f16 a[4:7], v[50:53], v[18:21], a[4:7]
	ds_read_b128 v[18:21], v30 offset:31616
	s_waitcnt lgkmcnt(2)
	v_mfma_f32_16x16x32_f16 a[8:11], v[50:53], v[22:25], a[8:11]
	ds_read_b128 v[22:25], v30 offset:31680
	s_waitcnt lgkmcnt(1)
	v_mfma_f32_16x16x32_f16 a[12:15], v[50:53], v[18:21], a[12:15]
	v_mbcnt_hi_u32_b32 v19, -1, v39
	v_lshlrev_b32_e32 v20, 3, v7
	v_lshlrev_b32_e32 v18, 3, v0
	s_waitcnt vmcnt(16)
	v_mfma_f32_16x16x32_f16 a[8:11], v[54:57], v[26:29], a[8:11]
	v_bfe_u32 v0, v0, 2, 2
	v_or_b32_e32 v0, v9, v0
	v_mul_u32_u24_e32 v0, 0x120, v0
	s_waitcnt lgkmcnt(0)
	v_mfma_f32_16x16x32_f16 a[12:15], v[54:57], v[22:25], a[12:15]
	v_and_or_b32 v0, v18, 24, v0
	v_mfma_f32_16x16x32_f16 a[0:3], v[54:57], v[14:17], a[0:3]
	v_and_b32_e32 v15, 64, v19
	v_xor_b32_e32 v14, 1, v19
	v_accvgpr_read_b32 v17, a8
	v_mfma_f32_16x16x32_f16 a[4:7], v[54:57], v[10:13], a[4:7]
	v_add_u32_e32 v12, 64, v15
	v_cmp_lt_i32_e32 vcc, v14, v12
	v_accvgpr_read_b32 v21, a12
	v_xor_b32_e32 v16, 2, v19
	v_cndmask_b32_e32 v13, v19, v14, vcc
	v_accvgpr_read_b32 v14, a0
	v_lshlrev_b32_e32 v13, 2, v13
	v_cmp_lt_i32_e32 vcc, v16, v12
	v_accvgpr_read_b32 v15, a4
	v_xor_b32_e32 v10, 4, v19
	v_cndmask_b32_e32 v16, v19, v16, vcc
	v_lshlrev_b32_e32 v16, 2, v16
	v_xor_b32_e32 v11, 8, v19
	v_cmp_lt_i32_e32 vcc, v10, v12
	v_accvgpr_read_b32 v26, a9
	v_accvgpr_read_b32 v22, a1
	v_cndmask_b32_e32 v10, v19, v10, vcc
	v_cmp_lt_i32_e32 vcc, v11, v12
	v_lshlrev_b32_e32 v10, 2, v10
	v_accvgpr_read_b32 v25, a5
	v_cndmask_b32_e32 v11, v19, v11, vcc
	v_lshlrev_b32_e32 v11, 2, v11
	v_accvgpr_read_b32 v41, a14
	v_accvgpr_read_b32 v23, a2
	v_accvgpr_read_b32 v42, a15
	v_accvgpr_read_b32 v24, a3
	s_waitcnt vmcnt(0)
	v_mov_b32_e32 v31, v68
	v_mov_b32_e32 v32, v69
	v_mov_b32_e32 v33, v70
	v_mov_b32_e32 v34, v71
	v_mov_b32_e32 v35, v72
	v_mov_b32_e32 v36, v73
	v_mov_b32_e32 v37, v74
	v_mov_b32_e32 v38, v75
	v_fmac_f32_e32 v31, 0x3e0293ee, v14
	s_waitcnt vmcnt(6)
	v_fmac_f32_e32 v32, 0x3e0293ee, v15
	s_waitcnt vmcnt(5)
	v_fmac_f32_e32 v33, 0x3e0293ee, v17
	s_waitcnt vmcnt(4)
	v_fmac_f32_e32 v34, 0x3e0293ee, v21
	v_max_f32_e32 v14, v33, v34
	v_max3_f32 v14, v31, v32, v14
	s_nop 1
	v_mov_b32_dpp v15, v14 quad_perm:[1,0,3,2] row_mask:0xf bank_mask:0xf
	s_waitcnt vmcnt(3)
	v_fmac_f32_e32 v35, 0x3e0293ee, v22
	s_waitcnt vmcnt(2)
	v_fmac_f32_e32 v36, 0x3e0293ee, v25
	s_waitcnt vmcnt(1)
	v_fmac_f32_e32 v37, 0x3e0293ee, v26
	s_waitcnt lgkmcnt(0)
	v_max_f32_e32 v15, v15, v15
	v_max_f32_e32 v14, v14, v15
	s_nop 1
	v_mov_b32_dpp v15, v14 quad_perm:[2,3,0,1] row_mask:0xf bank_mask:0xf
	s_waitcnt lgkmcnt(0)
	v_max_f32_e32 v12, v15, v15
	v_mov_b32_e32 v15, v76
	v_mov_b32_e32 v17, v77
	v_mov_b32_e32 v19, v78
	v_mov_b32_e32 v21, v79
	v_max_f32_e32 v12, v14, v12
	s_nop 1
	v_mov_b32_dpp v14, v12 row_half_mirror row_mask:0xf bank_mask:0xf
	s_waitcnt lgkmcnt(0)
	v_max_f32_e32 v14, v14, v14
	v_max_f32_e32 v12, v12, v14
	s_nop 1
	v_mov_b32_dpp v14, v12 row_mirror row_mask:0xf bank_mask:0xf
	s_waitcnt lgkmcnt(0)
	v_max_f32_e32 v14, v14, v14
	v_max_f32_e32 v12, v12, v14
	v_sub_f32_e32 v14, v31, v12
	v_sub_f32_e32 v27, v32, v12
	v_sub_f32_e32 v28, v33, v12
	v_sub_f32_e32 v12, v34, v12
	v_mov_b32_e32 v33, v80
	v_mov_b32_e32 v34, v81
	v_mov_b32_e32 v39, v82
	v_mov_b32_e32 v40, v83
	v_exp_f32_e32 v14, v14
	v_exp_f32_e32 v27, v27
	v_exp_f32_e32 v28, v28
	v_exp_f32_e32 v12, v12
	v_add_f32_e32 v29, 0, v14
	v_add_f32_e32 v29, v29, v27
	v_add_f32_e32 v29, v29, v28
	v_add_f32_e32 v29, v29, v12
	s_nop 1
	v_mov_b32_dpp v30, v29 quad_perm:[1,0,3,2] row_mask:0xf bank_mask:0xf
	v_accvgpr_read_b32 v31, a13
	s_waitcnt vmcnt(8)
	v_fmac_f32_e32 v38, 0x3e0293ee, v31
	v_max_f32_e32 v26, v37, v38
	v_max3_f32 v26, v35, v36, v26
	s_waitcnt lgkmcnt(0)
	v_add_f32_e32 v22, v29, v30
	s_nop 1
	v_mov_b32_dpp v29, v26 quad_perm:[1,0,3,2] row_mask:0xf bank_mask:0xf
	v_accvgpr_read_b32 v32, a10
	s_nop 1
	v_mov_b32_dpp v25, v22 quad_perm:[2,3,0,1] row_mask:0xf bank_mask:0xf
	v_accvgpr_read_b32 v30, a6
	v_accvgpr_read_b32 v4, a11
	s_waitcnt lgkmcnt(1)
	v_max_f32_e32 v29, v29, v29
	v_max_f32_e32 v26, v26, v29
	s_nop 1
	v_mov_b32_dpp v29, v26 quad_perm:[2,3,0,1] row_mask:0xf bank_mask:0xf
	s_waitcnt lgkmcnt(1)
	v_add_f32_e32 v22, v22, v25
	s_nop 1
	v_mov_b32_dpp v25, v22 row_half_mirror row_mask:0xf bank_mask:0xf
	v_accvgpr_read_b32 v31, a7
	v_cvt_f16_f32_e32 v14, v14
	s_waitcnt lgkmcnt(1)
	v_max_f32_e32 v5, v29, v29
	v_max_f32_e32 v5, v26, v5
	s_nop 1
	v_mov_b32_dpp v26, v5 row_half_mirror row_mask:0xf bank_mask:0xf
	s_waitcnt lgkmcnt(1)
	v_add_f32_e32 v22, v22, v25
	s_nop 1
	v_mov_b32_dpp v25, v22 row_mirror row_mask:0xf bank_mask:0xf
	v_cvt_f16_f32_e32 v27, v27
	v_cvt_f16_f32_e32 v28, v28
	s_waitcnt lgkmcnt(1)
	v_max_f32_e32 v26, v26, v26
	v_max_f32_e32 v5, v5, v26
	s_nop 1
	v_mov_b32_dpp v26, v5 row_mirror row_mask:0xf bank_mask:0xf
	s_waitcnt lgkmcnt(1)
	v_add_f32_e32 v22, v22, v25
	v_div_scale_f32 v25, s[6:7], v22, v22, 1.0
	v_rcp_f32_e32 v29, v25
	s_waitcnt lgkmcnt(0)
	v_max_f32_e32 v26, v26, v26
	v_max_f32_e32 v5, v5, v26
	v_sub_f32_e32 v26, v35, v5
	v_fma_f32 v43, -v25, v29, 1.0
	v_exp_f32_e32 v26, v26
	v_sub_f32_e32 v35, v36, v5
	v_fmac_f32_e32 v29, v43, v29
	v_exp_f32_e32 v35, v35
	v_sub_f32_e32 v36, v37, v5
	v_exp_f32_e32 v36, v36
	v_sub_f32_e32 v5, v38, v5
	v_exp_f32_e32 v5, v5
	v_add_f32_e32 v37, 0, v26
	v_add_f32_e32 v37, v37, v35
	v_add_f32_e32 v37, v37, v36
	v_add_f32_e32 v37, v37, v5
	s_waitcnt vmcnt(7)
	v_fmac_f32_e32 v15, 0x3e0293ee, v23
	s_waitcnt vmcnt(6)
	v_fmac_f32_e32 v17, 0x3e0293ee, v30
	s_waitcnt vmcnt(5)
	v_fmac_f32_e32 v19, 0x3e0293ee, v32
	s_waitcnt vmcnt(4)
	v_fmac_f32_e32 v21, 0x3e0293ee, v41
	v_max_f32_e32 v23, v19, v21
	v_max3_f32 v23, v15, v17, v23
	s_nop 1
	v_mov_b32_dpp v30, v23 quad_perm:[1,0,3,2] row_mask:0xf bank_mask:0xf
	v_div_scale_f32 v32, vcc, 1.0, v22, 1.0
	v_mul_f32_e32 v41, v32, v29
	v_fma_f32 v43, -v25, v41, v32
	s_waitcnt lgkmcnt(0)
	v_max_f32_e32 v30, v30, v30
	v_max_f32_e32 v23, v23, v30
	s_nop 1
	v_mov_b32_dpp v30, v23 quad_perm:[2,3,0,1] row_mask:0xf bank_mask:0xf
	v_fmac_f32_e32 v41, v43, v29
	v_fma_f32 v25, -v25, v41, v32
	v_div_fmas_f32 v25, v25, v29, v41
	s_nop 1
	v_mov_b32_dpp v38, v37 quad_perm:[1,0,3,2] row_mask:0xf bank_mask:0xf
	s_waitcnt lgkmcnt(1)
	v_max_f32_e32 v30, v30, v30
	v_max_f32_e32 v23, v23, v30
	s_nop 1
	v_mov_b32_dpp v30, v23 row_half_mirror row_mask:0xf bank_mask:0xf
	s_waitcnt vmcnt(3)
	v_fmac_f32_e32 v33, 0x3e0293ee, v24
	s_waitcnt vmcnt(1)
	v_fmac_f32_e32 v39, 0x3e0293ee, v4
	s_waitcnt vmcnt(0)
	v_fmac_f32_e32 v40, 0x3e0293ee, v42
	v_fmac_f32_e32 v34, 0x3e0293ee, v31
	s_waitcnt lgkmcnt(0)
	v_max_f32_e32 v30, v30, v30
	v_max_f32_e32 v23, v23, v30
	s_nop 1
	v_mov_b32_dpp v30, v23 row_mirror row_mask:0xf bank_mask:0xf
	v_max_f32_e32 v4, v39, v40
	v_max3_f32 v4, v33, v34, v4
	v_add_f32_e32 v37, v37, v38
	s_nop 1
	v_mov_b32_dpp v38, v37 quad_perm:[2,3,0,1] row_mask:0xf bank_mask:0xf
	s_waitcnt lgkmcnt(1)
	v_max_f32_e32 v29, v30, v30
	v_max_f32_e32 v23, v23, v29
	v_sub_f32_e32 v15, v15, v23
	v_sub_f32_e32 v17, v17, v23
	v_sub_f32_e32 v19, v19, v23
	v_sub_f32_e32 v21, v21, v23
	s_nop 1
	v_mov_b32_dpp v23, v4 quad_perm:[1,0,3,2] row_mask:0xf bank_mask:0xf
	s_waitcnt lgkmcnt(1)
	v_add_f32_e32 v37, v37, v38
	s_nop 1
	v_mov_b32_dpp v38, v37 row_half_mirror row_mask:0xf bank_mask:0xf
	v_exp_f32_e32 v15, v15
	v_exp_f32_e32 v17, v17
	s_waitcnt lgkmcnt(1)
	v_max_f32_e32 v23, v23, v23
	v_max_f32_e32 v4, v4, v23
	s_nop 1
	v_mov_b32_dpp v23, v4 quad_perm:[2,3,0,1] row_mask:0xf bank_mask:0xf
	s_waitcnt lgkmcnt(1)
	v_add_f32_e32 v32, v37, v38
	s_nop 1
	v_mov_b32_dpp v37, v32 row_mirror row_mask:0xf bank_mask:0xf
	v_div_fixup_f32 v22, v25, v22, 1.0
	v_exp_f32_e32 v19, v19
	s_waitcnt lgkmcnt(1)
	v_max_f32_e32 v23, v23, v23
	v_max_f32_e32 v4, v4, v23
	s_nop 1
	v_mov_b32_dpp v23, v4 row_half_mirror row_mask:0xf bank_mask:0xf
	s_waitcnt lgkmcnt(1)
	v_add_f32_e32 v25, v32, v37
	v_div_scale_f32 v29, s[6:7], v25, v25, 1.0
	v_exp_f32_e32 v21, v21
	s_waitcnt lgkmcnt(0)
	v_max_f32_e32 v23, v23, v23
	v_max_f32_e32 v4, v4, v23
	s_nop 1
	v_mov_b32_dpp v23, v4 row_mirror row_mask:0xf bank_mask:0xf
	v_rcp_f32_e32 v30, v29
	v_add_f32_e32 v32, 0, v15
	v_add_f32_e32 v24, v32, v17
	v_add_f32_e32 v24, v24, v19
	s_waitcnt lgkmcnt(0)
	v_max_f32_e32 v23, v23, v23
	v_max_f32_e32 v4, v4, v23
	v_add_f32_e32 v24, v24, v21
	v_sub_f32_e32 v23, v33, v4
	s_nop 1
	v_mov_b32_dpp v31, v24 quad_perm:[1,0,3,2] row_mask:0xf bank_mask:0xf
	v_fma_f32 v32, -v29, v30, 1.0
	v_exp_f32_e32 v23, v23
	v_sub_f32_e32 v33, v34, v4
	v_fmac_f32_e32 v30, v32, v30
	v_div_scale_f32 v32, vcc, 1.0, v25, 1.0
	v_exp_f32_e32 v33, v33
	v_sub_f32_e32 v34, v39, v4
	v_mul_f32_e32 v37, v32, v30
	v_exp_f32_e32 v34, v34
	v_sub_f32_e32 v4, v40, v4
	v_fma_f32 v38, -v29, v37, v32
	v_exp_f32_e32 v4, v4
	v_fmac_f32_e32 v37, v38, v30
	v_add_f32_e32 v38, 0, v23
	s_waitcnt lgkmcnt(0)
	v_add_f32_e32 v24, v24, v31
	v_add_f32_e32 v38, v38, v33
	s_nop 1
	v_mov_b32_dpp v31, v24 quad_perm:[2,3,0,1] row_mask:0xf bank_mask:0xf
	v_add_f32_e32 v38, v38, v34
	v_add_f32_e32 v38, v38, v4
	s_nop 1
	v_mov_b32_dpp v13, v38 quad_perm:[1,0,3,2] row_mask:0xf bank_mask:0xf
	v_fma_f32 v29, -v29, v37, v32
	s_waitcnt lgkmcnt(1)
	v_add_f32_e32 v24, v24, v31
	s_nop 1
	v_mov_b32_dpp v31, v24 row_half_mirror row_mask:0xf bank_mask:0xf
	v_div_fmas_f32 v29, v29, v30, v37
	s_waitcnt lgkmcnt(1)
	v_add_f32_e32 v13, v38, v13
	s_nop 1
	v_mov_b32_dpp v16, v13 quad_perm:[2,3,0,1] row_mask:0xf bank_mask:0xf
	v_div_fixup_f32 v25, v29, v25, 1.0
	s_waitcnt lgkmcnt(1)
	v_add_f32_e32 v24, v24, v31
	s_nop 1
	v_mov_b32_dpp v31, v24 row_mirror row_mask:0xf bank_mask:0xf
	v_cvt_f16_f32_e32 v12, v12
	s_waitcnt lgkmcnt(1)
	v_add_f32_e32 v13, v13, v16
	s_nop 1
	v_mov_b32_dpp v10, v13 row_half_mirror row_mask:0xf bank_mask:0xf
	v_cvt_f16_f32_e32 v26, v26
	s_waitcnt lgkmcnt(1)
	v_add_f32_e32 v24, v24, v31
	v_div_scale_f32 v30, s[6:7], v24, v24, 1.0
	v_rcp_f32_e32 v31, v30
	s_waitcnt lgkmcnt(0)
	v_add_f32_e32 v10, v13, v10
	s_nop 1
	v_mov_b32_dpp v11, v10 row_mirror row_mask:0xf bank_mask:0xf
	v_cvt_f16_f32_e32 v5, v5
	v_fma_f32 v16, -v30, v31, 1.0
	v_fmac_f32_e32 v31, v16, v31
	v_div_scale_f32 v16, vcc, 1.0, v24, 1.0
	v_mul_f32_e32 v13, v16, v31
	s_waitcnt lgkmcnt(0)
	v_add_f32_e32 v10, v10, v11
	v_fma_f32 v29, -v30, v13, v16
	v_div_scale_f32 v11, s[6:7], v10, v10, 1.0
	v_fmac_f32_e32 v13, v29, v31
	v_rcp_f32_e32 v29, v11
	v_fma_f32 v16, -v30, v13, v16
	v_div_fmas_f32 v13, v16, v31, v13
	v_div_fixup_f32 v13, v13, v24, 1.0
	v_fma_f32 v16, -v11, v29, 1.0
	v_fmac_f32_e32 v29, v16, v29
	s_movk_i32 s4, 0x1100
	v_mov_b32_e32 v16, 0x4800
	v_mad_u32_u24 v16, v1, s4, v16
	v_lshlrev_b32_e32 v24, 1, v8
	v_or_b32_e32 v30, v16, v24
	s_movk_i32 s4, 0x240
	v_mad_u32_u24 v31, v7, s4, v30
	s_waitcnt lgkmcnt(0)
	s_barrier
	ds_write_b16 v31, v14
	ds_write_b16 v31, v27 offset:32
	ds_write_b16 v31, v28 offset:64
	ds_write_b16 v31, v12 offset:96
	v_cvt_f16_f32_e32 v27, v35
	v_or_b32_e32 v12, 1, v9
	s_movk_i32 s4, 0x90
	v_cvt_f16_f32_e32 v28, v36
	v_mad_u32_u24 v14, v12, s4, v30
	ds_write_b16 v14, v26
	ds_write_b16 v14, v27 offset:32
	ds_write_b16 v14, v28 offset:64
	ds_write_b16 v14, v5 offset:96
	v_cvt_f16_f32_e32 v5, v15
	v_cvt_f16_f32_e32 v15, v17
	v_cvt_f16_f32_e32 v17, v19
	v_cvt_f16_f32_e32 v19, v21
	ds_write_b16 v14, v5 offset:144
	ds_write_b16 v14, v15 offset:176
	ds_write_b16 v14, v17 offset:208
	ds_write_b16 v14, v19 offset:240
	v_cvt_f16_f32_e32 v5, v23
	v_cvt_f16_f32_e32 v15, v33
	v_cvt_f16_f32_e32 v17, v34
	v_cvt_f16_f32_e32 v4, v4
	ds_write_b16 v14, v5 offset:288
	ds_write_b16 v14, v15 offset:320
	ds_write_b16 v14, v17 offset:352
	ds_write_b16 v14, v4 offset:384
	v_mul_u32_u24_e32 v4, 0x90, v8
	v_add3_u32 v4, v16, v4, v20
	s_waitcnt lgkmcnt(0)
	ds_read2_b64 v[36:39], v4 offset1:4
	ds_read2_b64 v[40:43], v4 offset0:8 offset1:12
	ds_read_b64_tr_b16 v[16:17], v0 offset:4608
	ds_read_b64_tr_b16 v[14:15], v0
	ds_read_b64_tr_b16 v[18:19], v0 offset:32
	ds_read_b64_tr_b16 v[30:31], v0 offset:64
	ds_read_b64_tr_b16 v[44:45], v0 offset:96
	ds_read_b64_tr_b16 v[20:21], v0 offset:4640
	ds_read_b64_tr_b16 v[32:33], v0 offset:4672
	ds_read_b64_tr_b16 v[46:47], v0 offset:4704
	s_waitcnt lgkmcnt(6)
	v_mfma_f32_16x16x32_f16 a[0:3], v[36:39], v[14:17], 0
	v_div_scale_f32 v4, vcc, 1.0, v10, 1.0
	v_mul_f32_e32 v5, v4, v29
	ds_read_b64_tr_b16 v[16:17], v0 offset:13824
	ds_read_b64_tr_b16 v[14:15], v0 offset:9216
	ds_read_b64_tr_b16 v[48:49], v0 offset:9248
	ds_read_b64_tr_b16 v[52:53], v0 offset:9280
	ds_read_b64_tr_b16 v[56:57], v0 offset:9312
	ds_read_b64_tr_b16 v[50:51], v0 offset:13856
	ds_read_b64_tr_b16 v[54:55], v0 offset:13888
	ds_read_b64_tr_b16 v[58:59], v0 offset:13920
	s_waitcnt lgkmcnt(6)
	v_mfma_f32_16x16x32_f16 a[0:3], v[40:43], v[14:17], a[0:3]
	v_fma_f32 v8, -v11, v5, v4
	v_fmac_f32_e32 v5, v8, v29
	v_fma_f32 v4, -v11, v5, v4
	v_mfma_f32_16x16x32_f16 a[4:7], v[36:39], v[18:21], 0
	v_div_fmas_f32 v4, v4, v29, v5
	v_div_fixup_f32 v4, v4, v10, 1.0
	s_movk_i32 s4, 0x1100
	v_mfma_f32_16x16x32_f16 a[8:11], v[36:39], v[30:33], 0
	v_accvgpr_read_b32 v5, a0
	v_accvgpr_read_b32 v8, a1
	v_accvgpr_read_b32 v9, a2
	s_waitcnt lgkmcnt(2)
	v_mfma_f32_16x16x32_f16 a[4:7], v[40:43], v[48:51], a[4:7]
	v_accvgpr_read_b32 v10, a3
	v_fma_mixlo_f16 v5, v5, v22, 0
	s_waitcnt lgkmcnt(1)
	v_mfma_f32_16x16x32_f16 a[0:3], v[40:43], v[52:55], a[8:11]
	v_mfma_f32_16x16x32_f16 a[8:11], v[36:39], v[44:47], 0
	ds_read_b64_tr_b16 v[28:29], v0 offset:4736
	ds_read_b64_tr_b16 v[26:27], v0 offset:128
	ds_read_b64_tr_b16 v[30:31], v0 offset:160
	ds_read_b64_tr_b16 v[44:45], v0 offset:192
	ds_read_b64_tr_b16 v[48:49], v0 offset:224
	ds_read_b64_tr_b16 v[32:33], v0 offset:4768
	ds_read_b64_tr_b16 v[46:47], v0 offset:4800
	ds_read_b64_tr_b16 v[50:51], v0 offset:4832
	v_accvgpr_read_b32 v11, a4
	v_accvgpr_read_b32 v14, a5
	v_accvgpr_read_b32 v15, a6
	v_accvgpr_read_b32 v16, a7
	v_accvgpr_read_b32 v17, a0
	v_accvgpr_read_b32 v18, a1
	s_waitcnt lgkmcnt(8)
	v_mfma_f32_16x16x32_f16 a[4:7], v[40:43], v[56:59], a[8:11]
	v_accvgpr_read_b32 v19, a3
	s_waitcnt lgkmcnt(6)
	v_mfma_f32_16x16x32_f16 a[8:11], v[36:39], v[26:29], 0
	ds_read_b64_tr_b16 v[28:29], v0 offset:13952
	ds_read_b64_tr_b16 v[26:27], v0 offset:9344
	ds_read_b64_tr_b16 v[52:53], v0 offset:9376
	ds_read_b64_tr_b16 v[56:57], v0 offset:9408
	ds_read_b64_tr_b16 v[60:61], v0 offset:9440
	ds_read_b64_tr_b16 v[54:55], v0 offset:13984
	ds_read_b64_tr_b16 v[58:59], v0 offset:14016
	ds_read_b64_tr_b16 v[62:63], v0 offset:14048
	v_accvgpr_read_b32 v0, a2
	v_accvgpr_read_b32 v20, a4
	s_waitcnt lgkmcnt(10)
	v_mfma_f32_16x16x32_f16 a[0:3], v[36:39], v[30:33], 0
	v_accvgpr_read_b32 v21, a5
	v_accvgpr_read_b32 v23, a6
	v_fma_mixlo_f16 v0, v0, v13, 0
	s_waitcnt lgkmcnt(2)
	v_mfma_f32_16x16x32_f16 a[0:3], v[40:43], v[52:55], a[0:3]
	v_mfma_f32_16x16x32_f16 a[8:11], v[40:43], v[26:29], a[8:11]
	v_accvgpr_read_b32 v26, a7
	v_mfma_f32_16x16x32_f16 a[4:7], v[36:39], v[44:47], 0
	s_nop 4
	v_accvgpr_read_b32 v31, a0
	v_accvgpr_read_b32 v32, a1
	v_accvgpr_read_b32 v33, a2
	v_accvgpr_read_b32 v34, a3
	v_mfma_f32_16x16x32_f16 a[0:3], v[36:39], v[48:51], 0
	v_accvgpr_read_b32 v27, a8
	v_accvgpr_read_b32 v28, a9
	v_accvgpr_read_b32 v29, a10
	s_waitcnt lgkmcnt(1)
	v_mfma_f32_16x16x32_f16 a[4:7], v[40:43], v[56:59], a[4:7]
	v_accvgpr_read_b32 v30, a11
	s_waitcnt lgkmcnt(0)
	v_mfma_f32_16x16x32_f16 a[0:3], v[40:43], v[60:63], a[0:3]
	v_mov_b32_e32 v43, 0x4800
	v_mad_u32_u24 v43, v1, s4, v43
	v_or_b32_e32 v1, v43, v24
	s_movk_i32 s4, 0x440
	v_mad_u32_u24 v24, v7, s4, v1
	ds_write_b16 v24, v5
	v_fma_mixlo_f16 v5, v8, v25, 0
	v_mad_u32_u24 v1, v12, s3, v1
	ds_write_b16 v1, v5
	v_fma_mixlo_f16 v5, v9, v13, 0
	ds_write_b16 v1, v5 offset:272
	v_fma_mixlo_f16 v5, v10, v4, 0
	ds_write_b16 v1, v5 offset:544
	v_fma_mixlo_f16 v5, v11, v22, 0
	ds_write_b16 v24, v5 offset:32
	v_fma_mixlo_f16 v5, v14, v25, 0
	ds_write_b16 v1, v5 offset:32
	v_fma_mixlo_f16 v5, v15, v13, 0
	ds_write_b16 v1, v5 offset:304
	v_fma_mixlo_f16 v5, v16, v4, 0
	ds_write_b16 v1, v5 offset:576
	v_fma_mixlo_f16 v5, v17, v22, 0
	ds_write_b16 v24, v5 offset:64
	ds_write_b16 v1, v0 offset:336
	v_fma_mixlo_f16 v0, v19, v4, 0
	v_fma_mixlo_f16 v5, v18, v25, 0
	ds_write_b16 v1, v0 offset:608
	v_fma_mixlo_f16 v0, v20, v22, 0
	ds_write_b16 v1, v5 offset:64
	ds_write_b16 v24, v0 offset:96
	v_fma_mixlo_f16 v0, v21, v25, 0
	ds_write_b16 v1, v0 offset:96
	v_fma_mixlo_f16 v0, v23, v13, 0
	ds_write_b16 v1, v0 offset:368
	v_fma_mixlo_f16 v0, v26, v4, 0
	ds_write_b16 v1, v0 offset:640
	v_fma_mixlo_f16 v0, v27, v22, 0
	ds_write_b16 v24, v0 offset:128
	v_fma_mixlo_f16 v0, v28, v25, 0
	ds_write_b16 v1, v0 offset:128
	v_fma_mixlo_f16 v0, v29, v13, 0
	ds_write_b16 v1, v0 offset:400
	v_fma_mixlo_f16 v0, v30, v4, 0
	ds_write_b16 v1, v0 offset:672
	v_fma_mixlo_f16 v0, v31, v22, 0
	ds_write_b16 v24, v0 offset:160
	v_fma_mixlo_f16 v0, v32, v25, 0
	ds_write_b16 v1, v0 offset:160
	v_fma_mixlo_f16 v0, v33, v13, 0
	v_accvgpr_read_b32 v35, a4
	ds_write_b16 v1, v0 offset:432
	v_fma_mixlo_f16 v0, v34, v4, 0
	v_accvgpr_read_b32 v36, a5
	ds_write_b16 v1, v0 offset:704
	v_fma_mixlo_f16 v0, v35, v22, 0
	v_accvgpr_read_b32 v37, a6
	ds_write_b16 v24, v0 offset:192
	v_fma_mixlo_f16 v0, v36, v25, 0
	v_accvgpr_read_b32 v38, a7
	ds_write_b16 v1, v0 offset:192
	v_fma_mixlo_f16 v0, v37, v13, 0
	v_accvgpr_read_b32 v39, a0
	ds_write_b16 v1, v0 offset:464
	v_fma_mixlo_f16 v0, v38, v4, 0
	v_accvgpr_read_b32 v40, a1
	ds_write_b16 v1, v0 offset:736
	v_fma_mixlo_f16 v0, v39, v22, 0
	v_accvgpr_read_b32 v41, a2
	ds_write_b16 v24, v0 offset:224
	v_fma_mixlo_f16 v0, v40, v25, 0
	v_accvgpr_read_b32 v42, a3
	ds_write_b16 v1, v0 offset:224
	v_fma_mixlo_f16 v0, v41, v13, 0
	ds_write_b16 v1, v0 offset:496
	v_fma_mixlo_f16 v0, v42, v4, 0
	ds_write_b16 v1, v0 offset:768
	v_lshl_or_b32 v4, s2, 6, v6
	s_movk_i32 s2, 0x600
	v_mov_b64_e32 v[0:1], s[8:9]
	v_mad_i64_i32 v[0:1], s[4:5], v4, s2, v[0:1]
	v_lshl_add_u64 v[0:1], v[0:1], 0, s[0:1]
	v_or_b32_e32 v4, v43, v2
	v_lshl_add_u64 v[0:1], v[0:1], 0, v[2:3]
	v_mul_u32_u24_e32 v2, 0x300, v7
	v_mad_u32_u24 v6, v7, s3, v4
	v_lshlrev_b32_e32 v2, 1, v2
	s_waitcnt lgkmcnt(0)
	ds_read_b128 v[8:11], v6
	v_lshl_add_u64 v[12:13], v[0:1], 0, v[2:3]
	ds_read_b128 v[0:3], v6 offset:1088
	s_movk_i32 s0, 0x1000
	v_add_co_u32_e32 v4, vcc, s0, v12
	s_waitcnt lgkmcnt(1)
	global_store_dwordx4 v[12:13], v[8:11], off nt
	v_addc_co_u32_e32 v5, vcc, 0, v13, vcc
	s_waitcnt lgkmcnt(0)
	global_store_dwordx4 v[4:5], v[0:3], off offset:2048 nt
	ds_read_b128 v[0:3], v6 offset:2176
	ds_read_b128 v[4:7], v6 offset:3264
	v_add_co_u32_e32 v8, vcc, 0x3000, v12
	s_nop 1
	v_addc_co_u32_e32 v9, vcc, 0, v13, vcc
	s_waitcnt lgkmcnt(1)
	global_store_dwordx4 v[8:9], v[0:3], off nt
	s_nop 1
	v_add_co_u32_e32 v0, vcc, 0x4000, v12
	s_nop 1
	v_addc_co_u32_e32 v1, vcc, 0, v13, vcc
	s_waitcnt lgkmcnt(0)
	global_store_dwordx4 v[0:1], v[4:7], off offset:2048 nt
	s_endpgm

	.amdhsa_kernel _Z6k_attnPKDF16_PKfPDF16_
		.amdhsa_group_segment_fixed_size 35840
		.amdhsa_private_segment_fixed_size 0
		.amdhsa_kernarg_size 24
		.amdhsa_user_sgpr_count 2
		.amdhsa_user_sgpr_dispatch_ptr 0
		.amdhsa_user_sgpr_queue_ptr 0
		.amdhsa_user_sgpr_kernarg_segment_ptr 1
		.amdhsa_user_sgpr_dispatch_id 0
		.amdhsa_user_sgpr_kernarg_preload_length 0
		.amdhsa_user_sgpr_kernarg_preload_offset 0
		.amdhsa_user_sgpr_private_segment_size 0
		.amdhsa_uses_dynamic_stack 0
		.amdhsa_enable_private_segment 0
		.amdhsa_system_sgpr_workgroup_id_x 1
		.amdhsa_system_sgpr_workgroup_id_y 0
		.amdhsa_system_sgpr_workgroup_id_z 0
		.amdhsa_system_sgpr_workgroup_info 0
		.amdhsa_system_vgpr_workitem_id 0
		.amdhsa_next_free_vgpr 104
		.amdhsa_next_free_sgpr 96
		.amdhsa_accum_offset 88
		.amdhsa_reserve_vcc 1
		.amdhsa_float_round_mode_32 0
		.amdhsa_float_round_mode_16_64 0
		.amdhsa_float_denorm_mode_32 3
		.amdhsa_float_denorm_mode_16_64 3
		.amdhsa_dx10_clamp 1
		.amdhsa_ieee_mode 1
		.amdhsa_fp16_overflow 0
		.amdhsa_tg_split 0
		.amdhsa_exception_fp_ieee_invalid_op 0
		.amdhsa_exception_fp_denorm_src 0
		.amdhsa_exception_fp_ieee_div_zero 0
		.amdhsa_exception_fp_ieee_overflow 0
		.amdhsa_exception_fp_ieee_underflow 0
		.amdhsa_exception_fp_ieee_inexact 0
		.amdhsa_exception_int_div_zero 0
	.end_amdhsa_kernel

amdhsa.kernels:
  - .agpr_count:     16
    .args:
      - .actual_access:  read_only
        .address_space:  global
        .offset:         0
        .size:           8
        .value_kind:     global_buffer
      - .actual_access:  read_only
        .address_space:  global
        .offset:         8
        .size:           8
        .value_kind:     global_buffer
      - .actual_access:  write_only
        .address_space:  global
        .offset:         16
        .size:           8
        .value_kind:     global_buffer
    .group_segment_fixed_size: 35840
    .kernarg_segment_align: 8
    .kernarg_segment_size: 24
    .language:       OpenCL C
    .language_version:
      - 2
      - 0
    .max_flat_workgroup_size: 256
    .name:           _Z6k_attnPKDF16_PKfPDF16_
    .private_segment_fixed_size: 0
    .sgpr_count:     16
    .sgpr_spill_count: 0
    .symbol:         _Z6k_attnPKDF16_PKfPDF16_.kd
    .uniform_work_group_size: 1
    .uses_dynamic_stack: false
    .vgpr_count:     104
    .vgpr_spill_count: 0
    .wavefront_size: 64
  - .agpr_count:     0
    .args:
      - .actual_access:  read_only
        .address_space:  global
        .offset:         0
        .size:           8
        .value_kind:     global_buffer
      - .actual_access:  read_only
        .address_space:  global
        .offset:         8
        .size:           8
        .value_kind:     global_buffer
      - .actual_access:  write_only
        .address_space:  global
        .offset:         16
        .size:           8
        .value_kind:     global_buffer
      - .actual_access:  write_only
        .address_space:  global
        .offset:         24
        .size:           8
        .value_kind:     global_buffer
      - .actual_access:  write_only
        .address_space:  global
        .offset:         32
        .size:           8
        .value_kind:     global_buffer
      - .actual_access:  write_only
        .address_space:  global
        .offset:         40
        .size:           8
        .value_kind:     global_buffer
    .group_segment_fixed_size: 0
    .kernarg_segment_align: 8
    .kernarg_segment_size: 48
    .language:       OpenCL C
    .language_version:
      - 2
      - 0
    .max_flat_workgroup_size: 256
    .name:           _Z11k_prep_miscPKiPKfPfPDv2_fS3_S3_
    .private_segment_fixed_size: 0
    .sgpr_count:     16
    .sgpr_spill_count: 0
    .symbol:         _Z11k_prep_miscPKiPKfPfPDv2_fS3_S3_.kd
    .uniform_work_group_size: 1
    .uses_dynamic_stack: false
    .vgpr_count:     6
    .vgpr_spill_count: 0
    .wavefront_size: 64
  - .agpr_count:     0
    .args:
      - .actual_access:  read_only
        .address_space:  global
        .offset:         0
        .size:           8
        .value_kind:     global_buffer
      - .actual_access:  write_only
        .address_space:  global
        .offset:         8
        .size:           8
        .value_kind:     global_buffer
    .group_segment_fixed_size: 0
    .kernarg_segment_align: 8
    .kernarg_segment_size: 16
    .language:       OpenCL C
    .language_version:
      - 2
      - 0
    .max_flat_workgroup_size: 256
    .name:           _Z7k_cvt_xPKfPDF16_
    .private_segment_fixed_size: 0
    .sgpr_count:     14
    .sgpr_spill_count: 0
    .symbol:         _Z7k_cvt_xPKfPDF16_.kd
    .uniform_work_group_size: 1
    .uses_dynamic_stack: false
    .vgpr_count:     12
    .vgpr_spill_count: 0
    .wavefront_size: 64
  - .agpr_count:     0
    .args:
      - .offset:         0
        .size:           176
        .value_kind:     by_value
    .group_segment_fixed_size: 9216
    .kernarg_segment_align: 8
    .kernarg_segment_size: 176
    .language:       OpenCL C
    .language_version:
      - 2
      - 0
    .max_flat_workgroup_size: 256
    .name:           _Z8k_wtrans8PrepArgs
    .private_segment_fixed_size: 0
    .sgpr_count:     44
    .sgpr_spill_count: 0
    .symbol:         _Z8k_wtrans8PrepArgs.kd
    .uniform_work_group_size: 1
    .uses_dynamic_stack: false
    .vgpr_count:     18
    .vgpr_spill_count: 0
    .wavefront_size: 64
  - .agpr_count:     0
    .args:
      - .offset:         0
        .size:           176
        .value_kind:     by_value
      - .actual_access:  read_only
        .address_space:  global
        .offset:         176
        .size:           8
        .value_kind:     global_buffer
      - .actual_access:  read_only
        .address_space:  global
        .offset:         184
        .size:           8
        .value_kind:     global_buffer
    .group_segment_fixed_size: 2048
    .kernarg_segment_align: 8
    .kernarg_segment_size: 192
    .language:       OpenCL C
    .language_version:
      - 2
      - 0
    .max_flat_workgroup_size: 256
    .name:           _Z8k_colvec8PrepArgsPKfS1_
    .private_segment_fixed_size: 0
    .sgpr_count:     38
    .sgpr_spill_count: 0
    .symbol:         _Z8k_colvec8PrepArgsPKfS1_.kd
    .uniform_work_group_size: 1
    .uses_dynamic_stack: false
    .vgpr_count:     114
    .vgpr_spill_count: 0
    .wavefront_size: 64
  - .agpr_count:     0
    .args:
      - .actual_access:  read_only
        .address_space:  global
        .offset:         0
        .size:           8
        .value_kind:     global_buffer
      - .actual_access:  write_only
        .address_space:  global
        .offset:         8
        .size:           8
        .value_kind:     global_buffer
    .group_segment_fixed_size: 0
    .kernarg_segment_align: 8
    .kernarg_segment_size: 16
    .language:       OpenCL C
    .language_version:
      - 2
      - 0
    .max_flat_workgroup_size: 256
    .name:           _Z9k_rowstatPKDv2_fPS_
    .private_segment_fixed_size: 0
    .sgpr_count:     16
    .sgpr_spill_count: 0
    .symbol:         _Z9k_rowstatPKDv2_fPS_.kd
    .uniform_work_group_size: 1
    .uses_dynamic_stack: false
    .vgpr_count:     28
    .vgpr_spill_count: 0
    .wavefront_size: 64
  - .agpr_count:     0
    .args:
      - .actual_access:  read_only
        .address_space:  global
        .offset:         0
        .size:           8
        .value_kind:     global_buffer
      - .actual_access:  read_only
        .address_space:  global
        .offset:         8
        .size:           8
        .value_kind:     global_buffer
      - .actual_access:  read_only
        .address_space:  global
        .offset:         16
        .size:           8
        .value_kind:     global_buffer
      - .actual_access:  read_only
        .address_space:  global
        .offset:         24
        .size:           8
        .value_kind:     global_buffer
      - .actual_access:  write_only
        .address_space:  global
        .offset:         32
        .size:           8
        .value_kind:     global_buffer
    .group_segment_fixed_size: 0
    .kernarg_segment_align: 8
    .kernarg_segment_size: 40
    .language:       OpenCL C
    .language_version:
      - 2
      - 0
    .max_flat_workgroup_size: 256
    .name:           _Z10k_final_lnPKDF16_PKDv2_fPKfS5_Pf
    .private_segment_fixed_size: 0
    .sgpr_count:     19
    .sgpr_spill_count: 0
    .symbol:         _Z10k_final_lnPKDF16_PKDv2_fPKfS5_Pf.kd
    .uniform_work_group_size: 1
    .uses_dynamic_stack: false
    .vgpr_count:     19
    .vgpr_spill_count: 0
    .wavefront_size: 64
  - .agpr_count:     0
    .args:
      - .offset:         0
        .size:           32
        .value_kind:     by_value
      - .offset:         32
        .size:           32
        .value_kind:     by_value
      - .offset:         64
        .size:           4
        .value_kind:     hidden_block_count_x
      - .offset:         68
        .size:           4
        .value_kind:     hidden_block_count_y
      - .offset:         72
        .size:           4
        .value_kind:     hidden_block_count_z
      - .offset:         76
        .size:           2
        .value_kind:     hidden_group_size_x
      - .offset:         78
        .size:           2
        .value_kind:     hidden_group_size_y
      - .offset:         80
        .size:           2
        .value_kind:     hidden_group_size_z
      - .offset:         82
        .size:           2
        .value_kind:     hidden_remainder_x
      - .offset:         84
        .size:           2
        .value_kind:     hidden_remainder_y
      - .offset:         86
        .size:           2
        .value_kind:     hidden_remainder_z
      - .offset:         104
        .size:           8
        .value_kind:     hidden_global_offset_x
      - .offset:         112
        .size:           8
        .value_kind:     hidden_global_offset_y
      - .offset:         120
        .size:           8
        .value_kind:     hidden_global_offset_z
      - .offset:         128
        .size:           2
        .value_kind:     hidden_grid_dims
      - .offset:         184
        .size:           4
        .value_kind:     hidden_dynamic_lds_size
    .group_segment_fixed_size: 0
    .kernarg_segment_align: 8
    .kernarg_segment_size: 320
    .language:       OpenCL C
    .language_version:
      - 2
      - 0
    .max_flat_workgroup_size: 512
    .name:           _Z6k_gemmIN2pg6EpiLinILi0EEELi768EEvNS0_4GemmET_
    .private_segment_fixed_size: 0
    .sgpr_count:     88
    .sgpr_spill_count: 0
    .symbol:         _Z6k_gemmIN2pg6EpiLinILi0EEELi768EEvNS0_4GemmET_.kd
    .uniform_work_group_size: 1
    .uses_dynamic_stack: false
    .vgpr_count:     254
    .vgpr_spill_count: 0
    .wavefront_size: 64
  - .agpr_count:     0
    .args:
      - .offset:         0
        .size:           32
        .value_kind:     by_value
      - .offset:         32
        .size:           56
        .value_kind:     by_value
      - .offset:         88
        .size:           4
        .value_kind:     hidden_block_count_x
      - .offset:         92
        .size:           4
        .value_kind:     hidden_block_count_y
      - .offset:         96
        .size:           4
        .value_kind:     hidden_block_count_z
      - .offset:         100
        .size:           2
        .value_kind:     hidden_group_size_x
      - .offset:         102
        .size:           2
        .value_kind:     hidden_group_size_y
      - .offset:         104
        .size:           2
        .value_kind:     hidden_group_size_z
      - .offset:         106
        .size:           2
        .value_kind:     hidden_remainder_x
      - .offset:         108
        .size:           2
        .value_kind:     hidden_remainder_y
      - .offset:         110
        .size:           2
        .value_kind:     hidden_remainder_z
      - .offset:         128
        .size:           8
        .value_kind:     hidden_global_offset_x
      - .offset:         136
        .size:           8
        .value_kind:     hidden_global_offset_y
      - .offset:         144
        .size:           8
        .value_kind:     hidden_global_offset_z
      - .offset:         152
        .size:           2
        .value_kind:     hidden_grid_dims
      - .offset:         208
        .size:           4
        .value_kind:     hidden_dynamic_lds_size
    .group_segment_fixed_size: 0
    .kernarg_segment_align: 8
    .kernarg_segment_size: 344
    .language:       OpenCL C
    .language_version:
      - 2
      - 0
    .max_flat_workgroup_size: 512
    .name:           _Z6k_gemmIN2pg6EpiResELi768EEvNS0_4GemmET_
    .private_segment_fixed_size: 0
    .sgpr_count:     108
    .sgpr_spill_count: 0
    .symbol:         _Z6k_gemmIN2pg6EpiResELi768EEvNS0_4GemmET_.kd
    .uniform_work_group_size: 1
    .uses_dynamic_stack: false
    .vgpr_count:     256
    .vgpr_spill_count: 0
    .wavefront_size: 64
  - .agpr_count:     0
    .args:
      - .offset:         0
        .size:           32
        .value_kind:     by_value
      - .offset:         32
        .size:           32
        .value_kind:     by_value
      - .offset:         64
        .size:           4
        .value_kind:     hidden_block_count_x
      - .offset:         68
        .size:           4
        .value_kind:     hidden_block_count_y
      - .offset:         72
        .size:           4
        .value_kind:     hidden_block_count_z
      - .offset:         76
        .size:           2
        .value_kind:     hidden_group_size_x
      - .offset:         78
        .size:           2
        .value_kind:     hidden_group_size_y
      - .offset:         80
        .size:           2
        .value_kind:     hidden_group_size_z
      - .offset:         82
        .size:           2
        .value_kind:     hidden_remainder_x
      - .offset:         84
        .size:           2
        .value_kind:     hidden_remainder_y
      - .offset:         86
        .size:           2
        .value_kind:     hidden_remainder_z
      - .offset:         104
        .size:           8
        .value_kind:     hidden_global_offset_x
      - .offset:         112
        .size:           8
        .value_kind:     hidden_global_offset_y
      - .offset:         120
        .size:           8
        .value_kind:     hidden_global_offset_z
      - .offset:         128
        .size:           2
        .value_kind:     hidden_grid_dims
      - .offset:         184
        .size:           4
        .value_kind:     hidden_dynamic_lds_size
    .group_segment_fixed_size: 0
    .kernarg_segment_align: 8
    .kernarg_segment_size: 320
    .language:       OpenCL C
    .language_version:
      - 2
      - 0
    .max_flat_workgroup_size: 512
    .name:           _Z6k_gemmIN2pg6EpiLinILi1EEELi768EEvNS0_4GemmET_
    .private_segment_fixed_size: 0
    .sgpr_count:     88
    .sgpr_spill_count: 0
    .symbol:         _Z6k_gemmIN2pg6EpiLinILi1EEELi768EEvNS0_4GemmET_.kd
    .uniform_work_group_size: 1
    .uses_dynamic_stack: false
    .vgpr_count:     254
    .vgpr_spill_count: 0
    .wavefront_size: 64
  - .agpr_count:     0
    .args:
      - .offset:         0
        .size:           32
        .value_kind:     by_value
      - .offset:         32
        .size:           56
        .value_kind:     by_value
      - .offset:         88
        .size:           4
        .value_kind:     hidden_block_count_x
      - .offset:         92
        .size:           4
        .value_kind:     hidden_block_count_y
      - .offset:         96
        .size:           4
        .value_kind:     hidden_block_count_z
      - .offset:         100
        .size:           2
        .value_kind:     hidden_group_size_x
      - .offset:         102
        .size:           2
        .value_kind:     hidden_group_size_y
      - .offset:         104
        .size:           2
        .value_kind:     hidden_group_size_z
      - .offset:         106
        .size:           2
        .value_kind:     hidden_remainder_x
      - .offset:         108
        .size:           2
        .value_kind:     hidden_remainder_y
      - .offset:         110
        .size:           2
        .value_kind:     hidden_remainder_z
      - .offset:         128
        .size:           8
        .value_kind:     hidden_global_offset_x
      - .offset:         136
        .size:           8
        .value_kind:     hidden_global_offset_y
      - .offset:         144
        .size:           8
        .value_kind:     hidden_global_offset_z
      - .offset:         152
        .size:           2
        .value_kind:     hidden_grid_dims
      - .offset:         208
        .size:           4
        .value_kind:     hidden_dynamic_lds_size
    .group_segment_fixed_size: 0
    .kernarg_segment_align: 8
    .kernarg_segment_size: 344
    .language:       OpenCL C
    .language_version:
      - 2
      - 0
    .max_flat_workgroup_size: 512
    .name:           _Z6k_gemmIN2pg6EpiResELi3072EEvNS0_4GemmET_
    .private_segment_fixed_size: 0
    .sgpr_count:     108
    .sgpr_spill_count: 0
    .symbol:         _Z6k_gemmIN2pg6EpiResELi3072EEvNS0_4GemmET_.kd
    .uniform_work_group_size: 1
    .uses_dynamic_stack: false
    .vgpr_count:     256
    .vgpr_spill_count: 0
    .wavefront_size: 64
